# stack + counted lgkmcnt per P.V MFMA (each MFMA waits only for the transposed V reads it consumes)
# baseline (speedup 1.0000x reference)
.LBB0_757:
	s_add_i32 s6, 0, 0x12000
	v_add_u32_e32 v199, s6, v170
	v_add_u32_e32 v204, s6, v171
	v_add_u32_e32 v205, s6, v172
	ds_read_b128 v[64:67], v180 offset:49152
	ds_read_b128 v[68:71], v180 offset:57344
	ds_read_b128 v[200:203], v181 offset:49152
	ds_read_b128 v[226:229], v181 offset:57344
	ds_read_b128 v[230:233], v182 offset:49152
	ds_read_b128 v[234:237], v182 offset:57344
	ds_read_b128 v[238:241], v183 offset:49152
	ds_read_b128 v[242:245], v183 offset:57344
	s_waitcnt lgkmcnt(7)
	v_mfma_f32_32x32x16_bf16 v[80:95], v[64:67], v[124:127], 0
	s_add_i32 s12, s64, -1
	s_sub_i32 s80, s11, 64
	s_cmp_lt_u32 s12, 3
	s_cselect_b32 s80, s10, s80
	s_mul_i32 s81, s80, 0xc00
	s_add_i32 s85, s82, 0x8000
	s_mov_b32 m0, s85
	s_add_i32 s85, s82, 0x10000
	buffer_load_dwordx4 v154, s[72:75], s81 offen lds
	v_exp_f32_e32 v216, v128
	v_add_f32_e32 v128, 0, v222
	v_add_f32_e32 v128, v224, v128
	v_add_f32_e32 v128, v220, v128
	v_add_f32_e32 v128, v223, v128
	v_add_f32_e32 v128, v219, v128
	v_add_f32_e32 v128, v221, v128
	s_waitcnt lgkmcnt(6)
	v_mfma_f32_32x32x16_bf16 v[64:79], v[68:71], v[124:127], 0
	s_mov_b32 m0, s85
	s_add_i32 s85, s82, 0xa000
	buffer_load_dwordx4 v155, s[72:75], s81 offen lds
	v_add_f32_e32 v128, v217, v128
	v_add_f32_e32 v128, v218, v128
	v_add_f32_e32 v128, v212, v128
	v_add_f32_e32 v128, v214, v128
	v_add_f32_e32 v128, v211, v128
	v_add_f32_e32 v128, v213, v128
	v_exp_f32_e32 v138, v138
	s_waitcnt lgkmcnt(5)
	v_mfma_f32_32x32x16_bf16 v[80:95], v[200:203], v[120:123], v[80:95]
	s_mov_b32 m0, s85
	s_add_i32 s81, s81, 0x18000
	buffer_load_dwordx4 v154, s[72:75], s81 offen lds
	v_add_f32_e32 v128, v208, v128
	v_exp_f32_e32 v139, v139
	v_add_f32_e32 v128, v210, v128
	v_exp_f32_e32 v164, v136
	v_add_f32_e32 v128, v207, v128
	v_exp_f32_e32 v137, v137
	v_add_f32_e32 v128, v209, v128
	s_waitcnt lgkmcnt(4)
	v_mfma_f32_32x32x16_bf16 v[64:79], v[226:229], v[120:123], v[64:79]
	s_lshl_b32 s81, s83, 11
	s_add_i32 s85, s82, 0x4000
	s_mov_b32 m0, s85
	s_add_i32 s85, s82, 0x6000
	buffer_load_dwordx4 v158, s[76:79], s81 offen lds
	ds_read_b128 v[200:203], v184 offset:49152
	ds_read_b128 v[226:229], v184 offset:57344
	v_exp_f32_e32 v165, v132
	v_add_f32_e32 v128, v138, v128
	v_add_f32_e32 v128, v139, v128
	v_exp_f32_e32 v206, v130
	v_add_f32_e32 v128, v164, v128
	v_exp_f32_e32 v215, v131
	s_waitcnt lgkmcnt(5)
	v_mfma_f32_32x32x16_bf16 v[80:95], v[230:233], v[116:119], v[80:95]
	s_mov_b32 m0, s85
	s_add_i32 s81, s81, 0x10000
	buffer_load_dwordx4 v158, s[76:79], s81 offen lds
	s_mov_b32 s84, s80
	v_add_f32_e32 v128, v137, v128
	v_add_f32_e32 v128, v165, v128
	v_exp_f32_e32 v225, v129
	v_exp_f32_e32 v162, v162
	v_exp_f32_e32 v163, v163
	v_exp_f32_e32 v160, v160
	v_exp_f32_e32 v161, v161
	s_waitcnt lgkmcnt(4)
	v_mfma_f32_32x32x16_bf16 v[64:79], v[234:237], v[116:119], v[64:79]
	ds_read_b128 v[230:233], v185 offset:49152
	ds_read_b128 v[234:237], v185 offset:57344
	v_cvt_pk_bf16_f32 v129, v220, v223
	v_cvt_pk_bf16_f32 v130, v219, v221
	v_cvt_pk_bf16_f32 v131, v217, v218
	v_cvt_pk_bf16_f32 v132, v212, v214
	v_cvt_pk_bf16_f32 v136, v138, v139
	v_cvt_pk_bf16_f32 v137, v164, v137
	s_waitcnt lgkmcnt(5)
	v_mfma_f32_32x32x16_bf16 v[80:95], v[238:241], v[112:115], v[80:95]
	v_cvt_pk_bf16_f32 v139, v206, v215
	v_permlane32_swap_b32_e32 v129, v131
	s_nop 0
	v_permlane32_swap_b32_e32 v137, v139
	s_waitcnt lgkmcnt(4)
	v_mfma_f32_32x32x16_bf16 v[64:79], v[242:245], v[112:115], v[64:79]
	ds_read_b128 v[238:241], v186 offset:49152
	ds_read_b128 v[242:245], v186 offset:57344
	s_waitcnt lgkmcnt(5)
	v_mfma_f32_32x32x16_bf16 v[80:95], v[200:203], v[108:111], v[80:95]
	s_waitcnt lgkmcnt(4)
	v_mfma_f32_32x32x16_bf16 v[64:79], v[226:229], v[108:111], v[64:79]
	ds_read_b128 v[200:203], v187 offset:49152
	ds_read_b128 v[226:229], v187 offset:57344
	s_waitcnt lgkmcnt(5)
	v_mfma_f32_32x32x16_bf16 v[80:95], v[230:233], v[104:107], v[80:95]
	s_waitcnt lgkmcnt(4)
	v_mfma_f32_32x32x16_bf16 v[64:79], v[234:237], v[104:107], v[64:79]
	ds_read_b128 v[230:233], v199
	ds_read_b128 v[234:237], v199 offset:4096
	ds_read_b128 v[246:249], v190
	s_waitcnt lgkmcnt(6)
	v_mfma_f32_32x32x16_bf16 v[80:95], v[238:241], v[100:103], v[80:95]
	s_waitcnt lgkmcnt(5)
	v_mfma_f32_32x32x16_bf16 v[64:79], v[242:245], v[100:103], v[64:79]
	ds_read_b128 v[238:241], v204
	ds_read_b128 v[242:245], v204 offset:4096
	ds_read_b128 v[250:253], v190 offset:1024
	v_add_u32_e32 v204, s6, v173
	s_waitcnt lgkmcnt(7)
	v_mfma_f32_32x32x16_bf16 v[80:95], v[200:203], v[96:99], v[80:95]
	s_waitcnt lgkmcnt(6)
	v_mfma_f32_32x32x16_bf16 v[64:79], v[226:229], v[96:99], v[64:79]
	ds_read_b128 v[200:203], v205
	ds_read_b128 v[226:229], v205 offset:4096
	s_waitcnt lgkmcnt(5)
	v_mfma_f32_32x32x16_bf16 v[80:95], v[230:233], v[246:249], v[80:95]
	s_waitcnt lgkmcnt(5)
	v_mfma_f32_32x32x16_bf16 v[64:79], v[234:237], v[246:249], v[64:79]
	ds_read_b128 v[230:233], v204
	ds_read_b128 v[234:237], v204 offset:4096
	ds_read_b128 v[246:249], v190 offset:2048
	s_waitcnt lgkmcnt(5)
	v_mfma_f32_32x32x16_bf16 v[80:95], v[238:241], v[250:253], v[80:95]
	s_waitcnt lgkmcnt(5)
	v_mfma_f32_32x32x16_bf16 v[64:79], v[242:245], v[250:253], v[64:79]
	ds_read_b128 v[250:253], v190 offset:3072
	s_waitcnt lgkmcnt(1)
	v_mfma_f32_32x32x16_bf16 v[80:95], v[200:203], v[246:249], v[80:95]
	v_exp_f32_e32 v205, v133
	v_cvt_pk_bf16_f32 v133, v211, v213
	v_cvt_pk_bf16_f32 v138, v165, v205
	v_add_f32_e32 v128, v205, v128
	v_add_f32_e32 v128, v206, v128
	v_add_f32_e32 v128, v215, v128
	s_waitcnt lgkmcnt(1)
	v_mfma_f32_32x32x16_bf16 v[64:79], v[226:229], v[246:249], v[64:79]
	v_add_f32_e32 v128, v216, v128
	v_add_f32_e32 v128, v225, v128
	v_add_f32_e32 v128, v162, v128
	v_add_f32_e32 v128, v163, v128
	v_add_f32_e32 v128, v160, v128
	v_add_f32_e32 v128, v161, v128
	s_waitcnt lgkmcnt(0)
	v_mfma_f32_32x32x16_bf16 v[80:95], v[230:233], v[250:253], v[80:95]
	v_exp_f32_e32 v226, v134
	v_exp_f32_e32 v227, v135
	v_cvt_pk_bf16_f32 v134, v208, v210
	v_cvt_pk_bf16_f32 v135, v207, v209
	v_add_f32_e32 v128, v226, v128
	v_add_f32_e32 v203, v227, v128
	v_mov_b32_e32 v204, v203
	s_waitcnt lgkmcnt(0)
	v_mfma_f32_32x32x16_bf16 v[64:79], v[234:237], v[250:253], v[64:79]
	s_nop 0
	v_permlane32_swap_b32_e32 v203, v204
	v_cvt_pk_bf16_f32 v128, v222, v224
	v_cvt_pk_bf16_f32 v208, v216, v225
	v_cvt_pk_bf16_f32 v209, v162, v163
	v_cvt_pk_bf16_f32 v210, v160, v161
	v_cvt_pk_bf16_f32 v211, v226, v227
	v_permlane32_swap_b32_e32 v132, v134
	v_permlane32_swap_b32_e32 v128, v130
	v_permlane32_swap_b32_e32 v133, v135
	v_permlane32_swap_b32_e32 v136, v138
	v_permlane32_swap_b32_e32 v208, v210
	v_permlane32_swap_b32_e32 v209, v211
	ds_read_b64_tr_b16 v[160:161], v167 offset:0
	ds_read_b64_tr_b16 v[162:163], v167 offset:0x800
	ds_read_b64_tr_b16 v[232:233], v167 offset:0x1000
	ds_read_b64_tr_b16 v[234:235], v167 offset:0x1800
	ds_read_b64_tr_b16 v[236:237], v167 offset:0x2000
	ds_read_b64_tr_b16 v[238:239], v167 offset:0x2800
	ds_read_b64_tr_b16 v[240:241], v167 offset:0x3000
	ds_read_b64_tr_b16 v[242:243], v167 offset:0x3800
	v_max_f32_e32 v164, v81, v81
	v_max_f32_e32 v165, v80, v80
	v_max_f32_e32 v164, v165, v164
	v_max3_f32 v164, v164, v82, v83
	v_max3_f32 v164, v164, v84, v85
	v_max3_f32 v164, v164, v86, v87
	v_max3_f32 v164, v164, v88, v89
	v_max3_f32 v164, v164, v90, v91
	v_max3_f32 v164, v164, v92, v93
	v_max3_f32 v164, v164, v94, v95
	s_waitcnt lgkmcnt(6)
	v_mfma_f32_32x32x16_bf16 v[16:31], v[128:131], v[160:163], v[16:31]
	v_max3_f32 v160, v164, v64, v65
	v_max3_f32 v160, v160, v66, v67
	v_max3_f32 v160, v160, v68, v69
	s_waitcnt lgkmcnt(4)
	v_mfma_f32_32x32x16_bf16 v[16:31], v[132:135], v[232:235], v[16:31]
	ds_read_b64_tr_b16 v[232:233], v167 offset:0x200
	ds_read_b64_tr_b16 v[234:235], v167 offset:0xa00
	v_max3_f32 v160, v160, v70, v71
	v_max3_f32 v160, v160, v72, v73
	v_max3_f32 v160, v160, v74, v75
	s_waitcnt lgkmcnt(4)
	v_mfma_f32_32x32x16_bf16 v[16:31], v[136:139], v[236:239], v[16:31]
	ds_read_b64_tr_b16 v[236:237], v167 offset:0x1200
	ds_read_b64_tr_b16 v[238:239], v167 offset:0x1a00
	ds_read_b64_tr_b16 v[244:245], v167 offset:0x2200
	ds_read_b64_tr_b16 v[246:247], v167 offset:0x2a00
	ds_read_b64_tr_b16 v[248:249], v167 offset:0x3200
	ds_read_b64_tr_b16 v[250:251], v167 offset:0x3a00
	v_max3_f32 v160, v160, v76, v77
	v_max3_f32 v160, v160, v78, v79
	v_mov_b32_e32 v161, v160
	s_waitcnt lgkmcnt(8)
	v_mfma_f32_32x32x16_bf16 v[16:31], v[208:211], v[240:243], v[16:31]
	v_max_f32_e32 v162, v198, v198
	v_permlane32_swap_b32_e32 v160, v161
	v_max_f32_e32 v161, v161, v161
	v_max_f32_e32 v160, v160, v160
	v_max_f32_e32 v160, v160, v161
	s_waitcnt lgkmcnt(6)
	v_mfma_f32_32x32x16_bf16 v[32:47], v[128:131], v[232:235], v[32:47]
	ds_read_b64_tr_b16 v[232:233], v167 offset:0x400
	ds_read_b64_tr_b16 v[234:235], v167 offset:0xc00
	v_sub_f32_e32 v161, v160, v198
	v_max_f32_e32 v160, v162, v160
	v_sub_f32_e32 v162, v198, v160
	v_mul_f32_e32 v162, 0x3dd53b94, v162
	v_exp_f32_e32 v162, v162
	s_waitcnt lgkmcnt(6)
	v_mfma_f32_32x32x16_bf16 v[32:47], v[132:135], v[236:239], v[32:47]
	ds_read_b64_tr_b16 v[236:237], v167 offset:0x1400
	ds_read_b64_tr_b16 v[238:239], v167 offset:0x1c00
	ds_read_b64_tr_b16 v[240:241], v167 offset:0x2400
	ds_read_b64_tr_b16 v[242:243], v167 offset:0x2c00
	v_cmp_ge_f32_e32 vcc, s48, v161
	s_cmp_eq_u64 vcc, exec
	s_cselect_b64 s[6:7], -1, 0
	v_cndmask_b32_e64 v206, v162, 1.0, s[6:7]
	v_cndmask_b32_e64 v160, v160, v198, s[6:7]
	v_mul_f32_e32 v205, 0xbdd53b94, v160
	v_cmp_gt_f32_e32 vcc, 1.0, v206
	s_waitcnt lgkmcnt(8)
	v_mfma_f32_32x32x16_bf16 v[32:47], v[136:139], v[244:247], v[32:47]
	ds_read_b64_tr_b16 v[244:245], v167 offset:0x3400
	ds_read_b64_tr_b16 v[246:247], v167 offset:0x3c00
	v_fmamk_f32 v87, v87, 0x3dd53b94, v205
	v_fmamk_f32 v80, v80, 0x3dd53b94, v205
	v_fmamk_f32 v81, v81, 0x3dd53b94, v205
	v_fmamk_f32 v82, v82, 0x3dd53b94, v205
	v_fmamk_f32 v83, v83, 0x3dd53b94, v205
	s_waitcnt lgkmcnt(8)
	v_mfma_f32_32x32x16_bf16 v[32:47], v[208:211], v[248:251], v[32:47]
	v_fmamk_f32 v84, v84, 0x3dd53b94, v205
	v_fmamk_f32 v85, v85, 0x3dd53b94, v205
	v_fmamk_f32 v86, v86, 0x3dd53b94, v205
	v_fmamk_f32 v88, v88, 0x3dd53b94, v205
	v_fmamk_f32 v89, v89, 0x3dd53b94, v205
	s_waitcnt lgkmcnt(6)
	v_mfma_f32_32x32x16_bf16 v[0:15], v[128:131], v[232:235], v[0:15]
	ds_read_b64_tr_b16 v[232:233], v167 offset:0x600
	ds_read_b64_tr_b16 v[234:235], v167 offset:0xe00
	v_fmamk_f32 v90, v90, 0x3dd53b94, v205
	v_fmamk_f32 v91, v91, 0x3dd53b94, v205
	v_fmamk_f32 v92, v92, 0x3dd53b94, v205
	v_fmamk_f32 v93, v93, 0x3dd53b94, v205
	v_fmamk_f32 v94, v94, 0x3dd53b94, v205
	s_waitcnt lgkmcnt(6)
	v_mfma_f32_32x32x16_bf16 v[0:15], v[132:135], v[236:239], v[0:15]
	ds_read_b64_tr_b16 v[236:237], v167 offset:0x1600
	ds_read_b64_tr_b16 v[238:239], v167 offset:0x1e00
	v_fmamk_f32 v95, v95, 0x3dd53b94, v205
	v_fmamk_f32 v215, v64, 0x3dd53b94, v205
	v_fmamk_f32 v216, v65, 0x3dd53b94, v205
	v_fmamk_f32 v217, v66, 0x3dd53b94, v205
	v_fmamk_f32 v218, v67, 0x3dd53b94, v205
	s_waitcnt lgkmcnt(6)
	v_mfma_f32_32x32x16_bf16 v[0:15], v[136:139], v[240:243], v[0:15]
	ds_read_b64_tr_b16 v[240:241], v167 offset:0x2600
	ds_read_b64_tr_b16 v[242:243], v167 offset:0x2e00
	ds_read_b64_tr_b16 v[248:249], v167 offset:0x3600
	ds_read_b64_tr_b16 v[250:251], v167 offset:0x3e00
	v_fmamk_f32 v219, v68, 0x3dd53b94, v205
	v_fmamk_f32 v212, v73, 0x3dd53b94, v205
	v_fmamk_f32 v213, v74, 0x3dd53b94, v205
	v_fmamk_f32 v214, v75, 0x3dd53b94, v205
	s_waitcnt lgkmcnt(8)
	v_mfma_f32_32x32x16_bf16 v[0:15], v[208:211], v[244:247], v[0:15]
	v_fmamk_f32 v207, v76, 0x3dd53b94, v205
	v_fmamk_f32 v220, v77, 0x3dd53b94, v205
	v_fmamk_f32 v221, v78, 0x3dd53b94, v205
	s_waitcnt lgkmcnt(6)
	v_mfma_f32_32x32x16_bf16 v[48:63], v[128:131], v[232:235], v[48:63]
	v_exp_f32_e32 v128, v80
	v_exp_f32_e32 v129, v82
	v_exp_f32_e32 v130, v84
	v_exp_f32_e32 v131, v86
	s_waitcnt lgkmcnt(4)
	v_mfma_f32_32x32x16_bf16 v[48:63], v[132:135], v[236:239], v[48:63]
	v_exp_f32_e32 v132, v88
	v_exp_f32_e32 v133, v90
	v_exp_f32_e32 v134, v92
	v_exp_f32_e32 v135, v94
	s_waitcnt lgkmcnt(2)
	v_mfma_f32_32x32x16_bf16 v[48:63], v[136:139], v[240:243], v[48:63]
	v_exp_f32_e32 v139, v89
	v_exp_f32_e32 v138, v91
	v_exp_f32_e32 v137, v93
	v_exp_f32_e32 v136, v95
	s_waitcnt lgkmcnt(0)
	v_mfma_f32_32x32x16_bf16 v[48:63], v[208:211], v[248:251], v[48:63]
	v_exp_f32_e32 v161, v87
	v_exp_f32_e32 v198, v81
	v_exp_f32_e32 v163, v83
	v_exp_f32_e32 v162, v85
	v_fmamk_f32 v208, v69, 0x3dd53b94, v205
	v_fmamk_f32 v209, v70, 0x3dd53b94, v205
	v_fmamk_f32 v210, v71, 0x3dd53b94, v205
	v_fmamk_f32 v211, v72, 0x3dd53b94, v205
	v_fmac_f32_e32 v205, 0x3dd53b94, v79
	s_cbranch_vccz .LBB0_761
	s_and_saveexec_b64 s[8:9], s[4:5]
	ds_write_b32 v189, v206 offset:128
	s_or_b64 exec, exec, s[8:9]
	s_waitcnt lgkmcnt(0)
	v_add_u32_e32 v248, s62, v169
	ds_read_b128 v[232:235], v248 offset:224
	ds_read_b128 v[236:239], v248 offset:192
	ds_read_b128 v[240:243], v248 offset:160
	ds_read_b128 v[244:247], v248 offset:128
	s_waitcnt lgkmcnt(3)
	v_pk_mul_f32 v[28:29], v[28:29], v[232:233]
	s_waitcnt lgkmcnt(2)
	v_pk_mul_f32 v[24:25], v[24:25], v[236:237]
	s_waitcnt lgkmcnt(1)
	v_pk_mul_f32 v[20:21], v[20:21], v[240:241]
	v_pk_mul_f32 v[30:31], v[30:31], v[234:235]
	v_pk_mul_f32 v[26:27], v[26:27], v[238:239]
	v_pk_mul_f32 v[22:23], v[22:23], v[242:243]
	s_waitcnt lgkmcnt(0)
	v_pk_mul_f32 v[18:19], v[18:19], v[246:247]
	v_pk_mul_f32 v[16:17], v[16:17], v[244:245]
	v_pk_mul_f32 v[44:45], v[44:45], v[232:233]
	v_pk_mul_f32 v[40:41], v[40:41], v[236:237]
	v_pk_mul_f32 v[36:37], v[36:37], v[240:241]
	v_pk_mul_f32 v[46:47], v[46:47], v[234:235]
	v_pk_mul_f32 v[42:43], v[42:43], v[238:239]
	v_pk_mul_f32 v[38:39], v[38:39], v[242:243]
	v_pk_mul_f32 v[34:35], v[34:35], v[246:247]
	v_pk_mul_f32 v[32:33], v[32:33], v[244:245]
	v_pk_mul_f32 v[12:13], v[12:13], v[232:233]
	v_pk_mul_f32 v[8:9], v[8:9], v[236:237]
	v_pk_mul_f32 v[4:5], v[4:5], v[240:241]
	v_pk_mul_f32 v[14:15], v[14:15], v[234:235]
	v_pk_mul_f32 v[10:11], v[10:11], v[238:239]
	v_pk_mul_f32 v[6:7], v[6:7], v[242:243]
	v_pk_mul_f32 v[2:3], v[2:3], v[246:247]
	v_pk_mul_f32 v[0:1], v[0:1], v[244:245]
	v_pk_mul_f32 v[60:61], v[60:61], v[232:233]
	v_pk_mul_f32 v[56:57], v[56:57], v[236:237]
	v_pk_mul_f32 v[52:53], v[52:53], v[240:241]
	v_pk_mul_f32 v[62:63], v[62:63], v[234:235]
	v_pk_mul_f32 v[58:59], v[58:59], v[238:239]
	v_pk_mul_f32 v[54:55], v[54:55], v[242:243]
	v_pk_mul_f32 v[50:51], v[50:51], v[246:247]
	v_pk_mul_f32 v[48:49], v[48:49], v[244:245]
.LBB0_761:
	s_waitcnt vmcnt(0) lgkmcnt(0)
	s_barrier
	ds_read_b128 v[64:67], v180 offset:32768
	ds_read_b128 v[68:71], v180 offset:40960
	ds_read_b128 v[222:225], v181 offset:32768
	ds_read_b128 v[226:229], v181 offset:40960
	ds_read_b128 v[230:233], v182 offset:32768
	ds_read_b128 v[234:237], v182 offset:40960
	ds_read_b128 v[238:241], v183 offset:32768
	ds_read_b128 v[242:245], v183 offset:40960
	v_exp_f32_e32 v164, v215
	v_add_f32_e32 v215, 0, v128
	s_waitcnt lgkmcnt(7)
	v_mfma_f32_32x32x16_bf16 v[80:95], v[64:67], v[124:127], 0
	s_add_i32 s80, s10, 64
	s_cmp_lt_u32 s12, 2
	s_cselect_b32 s80, s80, s11
	s_mul_i32 s81, s80, 0xc00
	s_add_i32 s85, s82, 0xc000
	s_mov_b32 m0, s85
	s_add_i32 s85, s82, 0x12000
	buffer_load_dwordx4 v154, s[72:75], s81 offen lds
	v_add_f32_e32 v215, v198, v215
	v_add_f32_e32 v215, v129, v215
	v_add_f32_e32 v215, v163, v215
	v_add_f32_e32 v215, v130, v215
	v_add_f32_e32 v215, v162, v215
	v_add_f32_e32 v215, v131, v215
	v_add_f32_e32 v215, v161, v215
	s_waitcnt lgkmcnt(6)
	v_mfma_f32_32x32x16_bf16 v[64:79], v[68:71], v[124:127], 0
	s_mov_b32 m0, s85
	s_add_i32 s85, s82, 0xe000
	buffer_load_dwordx4 v155, s[72:75], s81 offen lds
	v_add_f32_e32 v215, v132, v215
	v_add_f32_e32 v215, v139, v215
	v_add_f32_e32 v215, v133, v215
	v_add_f32_e32 v215, v138, v215
	v_add_f32_e32 v215, v134, v215
	v_exp_f32_e32 v165, v216
	v_add_f32_e32 v215, v137, v215
	s_waitcnt lgkmcnt(5)
	v_mfma_f32_32x32x16_bf16 v[80:95], v[222:225], v[120:123], v[80:95]
	s_mov_b32 m0, s85
	s_add_i32 s81, s81, 0x18000
	buffer_load_dwordx4 v154, s[72:75], s81 offen lds
	v_exp_f32_e32 v217, v217
	v_add_f32_e32 v215, v135, v215
	v_exp_f32_e32 v218, v218
	v_add_f32_e32 v215, v136, v215
	v_exp_f32_e32 v219, v219
	v_add_f32_e32 v215, v164, v215
	v_exp_f32_e32 v208, v208
	s_waitcnt lgkmcnt(4)
	v_mfma_f32_32x32x16_bf16 v[64:79], v[226:229], v[120:123], v[64:79]
	s_lshl_b32 s81, s84, 11
	s_add_i32 s85, s82, 0x0
	s_mov_b32 m0, s85
	s_add_i32 s85, s82, 0x2000
	buffer_load_dwordx4 v158, s[76:79], s81 offen lds
	ds_read_b128 v[222:225], v184 offset:32768
	ds_read_b128 v[226:229], v184 offset:40960
	v_add_f32_e32 v215, v165, v215
	v_exp_f32_e32 v209, v209
	v_add_f32_e32 v215, v217, v215
	v_exp_f32_e32 v210, v210
	v_add_f32_e32 v215, v218, v215
	v_exp_f32_e32 v211, v211
	s_waitcnt lgkmcnt(5)
	v_mfma_f32_32x32x16_bf16 v[80:95], v[230:233], v[116:119], v[80:95]
	s_mov_b32 m0, s85
	s_add_i32 s81, s81, 0x10000
	buffer_load_dwordx4 v158, s[76:79], s81 offen lds
	s_mov_b32 s83, s80
	v_add_f32_e32 v215, v219, v215
	v_exp_f32_e32 v212, v212
	v_add_f32_e32 v215, v208, v215
	v_exp_f32_e32 v213, v213
	v_add_f32_e32 v215, v209, v215
	v_exp_f32_e32 v214, v214
	v_add_f32_e32 v215, v210, v215
	s_waitcnt lgkmcnt(4)
	v_mfma_f32_32x32x16_bf16 v[64:79], v[234:237], v[116:119], v[64:79]
	ds_read_b128 v[230:233], v185 offset:32768
	ds_read_b128 v[234:237], v185 offset:40960
	v_exp_f32_e32 v207, v207
	v_add_f32_e32 v215, v211, v215
	v_exp_f32_e32 v220, v220
	v_add_f32_e32 v215, v212, v215
	v_exp_f32_e32 v221, v221
	v_add_f32_e32 v215, v213, v215
	s_waitcnt lgkmcnt(5)
	v_mfma_f32_32x32x16_bf16 v[80:95], v[238:241], v[112:115], v[80:95]
	v_exp_f32_e32 v205, v205
	v_add_f32_e32 v215, v214, v215
	v_add_f32_e32 v215, v207, v215
	v_add_f32_e32 v215, v220, v215
	v_add_f32_e32 v215, v221, v215
	v_add_f32_e32 v215, v205, v215
	v_mov_b32_e32 v216, v215
	s_waitcnt lgkmcnt(4)
	v_mfma_f32_32x32x16_bf16 v[64:79], v[242:245], v[112:115], v[64:79]
	ds_read_b128 v[238:241], v186 offset:32768
	ds_read_b128 v[242:245], v186 offset:40960
	v_permlane32_swap_b32_e32 v215, v216
	v_cvt_pk_bf16_f32 v128, v128, v198
	v_cvt_pk_bf16_f32 v129, v129, v163
	v_cvt_pk_bf16_f32 v130, v130, v162
	v_cvt_pk_bf16_f32 v131, v131, v161
	s_waitcnt lgkmcnt(5)
	v_mfma_f32_32x32x16_bf16 v[80:95], v[222:225], v[108:111], v[80:95]
	v_cvt_pk_bf16_f32 v132, v132, v139
	v_cvt_pk_bf16_f32 v133, v133, v138
	v_cvt_pk_bf16_f32 v134, v134, v137
	v_cvt_pk_bf16_f32 v135, v135, v136
	v_cvt_pk_bf16_f32 v136, v164, v165
	v_cvt_pk_bf16_f32 v137, v217, v218
	v_cvt_pk_bf16_f32 v138, v219, v208
	s_waitcnt lgkmcnt(4)
	v_mfma_f32_32x32x16_bf16 v[64:79], v[226:229], v[108:111], v[64:79]
	ds_read_b128 v[222:225], v187 offset:32768
	ds_read_b128 v[226:229], v187 offset:40960
	v_cvt_pk_bf16_f32 v139, v209, v210
	v_cvt_pk_bf16_f32 v208, v211, v212
	v_cvt_pk_bf16_f32 v209, v213, v214
	v_cvt_pk_bf16_f32 v210, v207, v220
	v_cvt_pk_bf16_f32 v211, v221, v205
	v_permlane32_swap_b32_e32 v128, v130
	s_waitcnt lgkmcnt(5)
	v_mfma_f32_32x32x16_bf16 v[80:95], v[230:233], v[104:107], v[80:95]
	v_permlane32_swap_b32_e32 v129, v131
	v_permlane32_swap_b32_e32 v132, v134
	v_permlane32_swap_b32_e32 v133, v135
	v_permlane32_swap_b32_e32 v136, v138
	s_waitcnt lgkmcnt(4)
	v_mfma_f32_32x32x16_bf16 v[64:79], v[234:237], v[104:107], v[64:79]
	ds_read_b128 v[230:233], v191
	ds_read_b128 v[234:237], v191 offset:4096
	ds_read_b128 v[246:249], v190
	v_permlane32_swap_b32_e32 v137, v139
	v_permlane32_swap_b32_e32 v208, v210
	v_permlane32_swap_b32_e32 v209, v211
	s_waitcnt lgkmcnt(6)
	v_mfma_f32_32x32x16_bf16 v[80:95], v[238:241], v[100:103], v[80:95]
	s_waitcnt lgkmcnt(5)
	v_mfma_f32_32x32x16_bf16 v[64:79], v[242:245], v[100:103], v[64:79]
	ds_read_b128 v[238:241], v192
	ds_read_b128 v[242:245], v192 offset:4096
	ds_read_b128 v[250:253], v190 offset:1024
	s_waitcnt lgkmcnt(7)
	v_mfma_f32_32x32x16_bf16 v[80:95], v[222:225], v[96:99], v[80:95]
	s_waitcnt lgkmcnt(6)
	v_mfma_f32_32x32x16_bf16 v[64:79], v[226:229], v[96:99], v[64:79]
	ds_read_b128 v[222:225], v193
	ds_read_b128 v[226:229], v193 offset:4096
	s_waitcnt lgkmcnt(5)
	v_mfma_f32_32x32x16_bf16 v[80:95], v[230:233], v[246:249], v[80:95]
	s_waitcnt lgkmcnt(5)
	v_mfma_f32_32x32x16_bf16 v[64:79], v[234:237], v[246:249], v[64:79]
	ds_read_b128 v[230:233], v194
	ds_read_b128 v[234:237], v194 offset:4096
	ds_read_b128 v[246:249], v190 offset:2048
	s_waitcnt lgkmcnt(5)
	v_mfma_f32_32x32x16_bf16 v[80:95], v[238:241], v[250:253], v[80:95]
	s_waitcnt lgkmcnt(5)
	v_mfma_f32_32x32x16_bf16 v[64:79], v[242:245], v[250:253], v[64:79]
	ds_read_b128 v[250:253], v190 offset:3072
	s_waitcnt lgkmcnt(1)
	v_mfma_f32_32x32x16_bf16 v[80:95], v[222:225], v[246:249], v[80:95]
	s_waitcnt lgkmcnt(1)
	v_mfma_f32_32x32x16_bf16 v[64:79], v[226:229], v[246:249], v[64:79]
	s_waitcnt lgkmcnt(0)
	v_mfma_f32_32x32x16_bf16 v[80:95], v[230:233], v[250:253], v[80:95]
	s_waitcnt lgkmcnt(0)
	v_mfma_f32_32x32x16_bf16 v[64:79], v[234:237], v[250:253], v[64:79]
	ds_read_b64_tr_b16 v[238:239], v174 offset:0
	ds_read_b64_tr_b16 v[240:241], v174 offset:0x800
	ds_read_b64_tr_b16 v[242:243], v174 offset:0x1000
	ds_read_b64_tr_b16 v[244:245], v174 offset:0x1800
	ds_read_b64_tr_b16 v[246:247], v174 offset:0x2000
	ds_read_b64_tr_b16 v[248:249], v174 offset:0x2800
	ds_read_b64_tr_b16 v[250:251], v174 offset:0x3000
	ds_read_b64_tr_b16 v[252:253], v174 offset:0x3800
	s_nop 3
	v_max_f32_e32 v161, v81, v81
	v_max_f32_e32 v162, v80, v80
	v_max_f32_e32 v161, v162, v161
	v_max3_f32 v161, v161, v82, v83
	v_max3_f32 v161, v161, v84, v85
	v_max3_f32 v161, v161, v86, v87
	v_max3_f32 v161, v161, v88, v89
	v_max3_f32 v161, v161, v90, v91
	v_max3_f32 v161, v161, v92, v93
	v_max3_f32 v161, v161, v94, v95
	s_waitcnt lgkmcnt(6)
	v_mfma_f32_32x32x16_bf16 v[16:31], v[128:131], v[238:241], v[16:31]
	ds_read_b64_tr_b16 v[238:239], v174 offset:0x200
	ds_read_b64_tr_b16 v[240:241], v174 offset:0xa00
	v_max3_f32 v161, v161, v64, v65
	v_max3_f32 v161, v161, v66, v67
	v_max3_f32 v161, v161, v68, v69
	s_waitcnt lgkmcnt(6)
	v_mfma_f32_32x32x16_bf16 v[16:31], v[132:135], v[242:245], v[16:31]
	ds_read_b64_tr_b16 v[242:243], v174 offset:0x1200
	ds_read_b64_tr_b16 v[244:245], v174 offset:0x1a00
	v_max3_f32 v161, v161, v70, v71
	v_max3_f32 v161, v161, v72, v73
	v_max3_f32 v161, v161, v74, v75
	s_waitcnt lgkmcnt(6)
	v_mfma_f32_32x32x16_bf16 v[16:31], v[136:139], v[246:249], v[16:31]
	ds_read_b64_tr_b16 v[246:247], v174 offset:0x2200
	ds_read_b64_tr_b16 v[248:249], v174 offset:0x2a00
	ds_read_b64_tr_b16 v[162:163], v174 offset:0x3200
	ds_read_b64_tr_b16 v[164:165], v174 offset:0x3a00
	v_max3_f32 v161, v161, v76, v77
	v_max3_f32 v161, v161, v78, v79
	v_mov_b32_e32 v198, v161
	s_waitcnt lgkmcnt(8)
	v_mfma_f32_32x32x16_bf16 v[16:31], v[208:211], v[250:253], v[16:31]
	v_max_f32_e32 v205, v160, v160
	v_permlane32_swap_b32_e32 v161, v198
	v_max_f32_e32 v198, v198, v198
	v_max_f32_e32 v161, v161, v161
	v_max_f32_e32 v161, v161, v198
	s_waitcnt lgkmcnt(6)
	v_mfma_f32_32x32x16_bf16 v[32:47], v[128:131], v[238:241], v[32:47]
	ds_read_b64_tr_b16 v[238:239], v174 offset:0x400
	ds_read_b64_tr_b16 v[240:241], v174 offset:0xc00
	v_sub_f32_e32 v198, v161, v160
	v_max_f32_e32 v161, v205, v161
	v_sub_f32_e32 v205, v160, v161
	v_mul_f32_e32 v205, 0x3dd53b94, v205
	v_exp_f32_e32 v205, v205
	s_waitcnt lgkmcnt(6)
	v_mfma_f32_32x32x16_bf16 v[32:47], v[132:135], v[242:245], v[32:47]
	ds_read_b64_tr_b16 v[242:243], v174 offset:0x1400
	ds_read_b64_tr_b16 v[244:245], v174 offset:0x1c00
	v_cmp_ge_f32_e32 vcc, s48, v198
	s_cmp_eq_u64 vcc, exec
	s_cselect_b64 s[6:7], -1, 0
	v_cndmask_b32_e64 v205, v205, 1.0, s[6:7]
	v_cndmask_b32_e64 v198, v161, v160, s[6:7]
	v_mul_f32_e32 v236, 0xbdd53b94, v198
	v_mov_b32_e32 v237, v236
	v_cmp_gt_f32_e32 vcc, 1.0, v205
	s_waitcnt lgkmcnt(6)
	v_mfma_f32_32x32x16_bf16 v[32:47], v[136:139], v[246:249], v[32:47]
	ds_read_b64_tr_b16 v[246:247], v174 offset:0x2400
	ds_read_b64_tr_b16 v[248:249], v174 offset:0x2c00
	ds_read_b64_tr_b16 v[250:251], v174 offset:0x3400
	ds_read_b64_tr_b16 v[252:253], v174 offset:0x3c00
	v_fmamk_f32 v80, v80, 0x3dd53b94, v236
	v_fmamk_f32 v81, v81, 0x3dd53b94, v236
	v_fmamk_f32 v82, v82, 0x3dd53b94, v236
	v_fmamk_f32 v83, v83, 0x3dd53b94, v236
	s_waitcnt lgkmcnt(8)
	v_mfma_f32_32x32x16_bf16 v[32:47], v[208:211], v[162:165], v[32:47]
	v_fmamk_f32 v84, v84, 0x3dd53b94, v236
	v_fmamk_f32 v85, v85, 0x3dd53b94, v236
	v_fmamk_f32 v86, v86, 0x3dd53b94, v236
	v_fmamk_f32 v87, v87, 0x3dd53b94, v236
	s_waitcnt lgkmcnt(6)
	v_mfma_f32_32x32x16_bf16 v[0:15], v[128:131], v[238:241], v[0:15]
	ds_read_b64_tr_b16 v[162:163], v174 offset:0x600
	ds_read_b64_tr_b16 v[164:165], v174 offset:0xe00
	ds_read_b64_tr_b16 v[238:239], v174 offset:0x1600
	ds_read_b64_tr_b16 v[240:241], v174 offset:0x1e00
	v_fmamk_f32 v88, v88, 0x3dd53b94, v236
	v_fmamk_f32 v89, v89, 0x3dd53b94, v236
	v_fmamk_f32 v90, v90, 0x3dd53b94, v236
	v_fmamk_f32 v91, v91, 0x3dd53b94, v236
	s_waitcnt lgkmcnt(8)
	v_mfma_f32_32x32x16_bf16 v[0:15], v[132:135], v[242:245], v[0:15]
	ds_read_b64_tr_b16 v[242:243], v174 offset:0x2600
	ds_read_b64_tr_b16 v[244:245], v174 offset:0x2e00
	v_fmamk_f32 v92, v92, 0x3dd53b94, v236
	v_fmamk_f32 v93, v93, 0x3dd53b94, v236
	v_fmamk_f32 v94, v94, 0x3dd53b94, v236
	v_fmamk_f32 v95, v95, 0x3dd53b94, v236
	s_waitcnt lgkmcnt(8)
	v_mfma_f32_32x32x16_bf16 v[0:15], v[136:139], v[246:249], v[0:15]
	ds_read_b64_tr_b16 v[246:247], v174 offset:0x3600
	ds_read_b64_tr_b16 v[248:249], v174 offset:0x3e00
	v_exp_f32_e32 v222, v80
	v_exp_f32_e32 v224, v81
	v_exp_f32_e32 v220, v82
	s_waitcnt lgkmcnt(8)
	v_mfma_f32_32x32x16_bf16 v[0:15], v[208:211], v[250:253], v[0:15]
	v_exp_f32_e32 v223, v83
	v_exp_f32_e32 v219, v84
	v_exp_f32_e32 v221, v85
	s_waitcnt lgkmcnt(6)
	v_mfma_f32_32x32x16_bf16 v[48:63], v[128:131], v[162:165], v[48:63]
	v_exp_f32_e32 v217, v86
	v_exp_f32_e32 v218, v87
	v_exp_f32_e32 v212, v88
	v_pk_fma_f32 v[130:131], v[70:71], s[28:29], v[236:237] op_sel_hi:[1,0,0]
	v_pk_fma_f32 v[128:129], v[72:73], s[28:29], v[236:237] op_sel_hi:[1,0,0]
	s_waitcnt lgkmcnt(4)
	v_mfma_f32_32x32x16_bf16 v[48:63], v[132:135], v[238:241], v[48:63]
	v_exp_f32_e32 v214, v89
	v_exp_f32_e32 v213, v91
	v_exp_f32_e32 v207, v94
	v_pk_fma_f32 v[132:133], v[68:69], s[28:29], v[236:237] op_sel_hi:[1,0,0]
	v_pk_fma_f32 v[134:135], v[78:79], s[28:29], v[236:237] op_sel_hi:[1,0,0]
	s_waitcnt lgkmcnt(2)
	v_mfma_f32_32x32x16_bf16 v[48:63], v[136:139], v[242:245], v[48:63]
	v_pk_fma_f32 v[138:139], v[64:65], s[28:29], v[236:237] op_sel_hi:[1,0,0]
	v_pk_fma_f32 v[136:137], v[66:67], s[28:29], v[236:237] op_sel_hi:[1,0,0]
	v_pk_fma_f32 v[162:163], v[74:75], s[28:29], v[236:237] op_sel_hi:[1,0,0]
	v_pk_fma_f32 v[160:161], v[76:77], s[28:29], v[236:237] op_sel_hi:[1,0,0]
	s_waitcnt lgkmcnt(0)
	v_mfma_f32_32x32x16_bf16 v[48:63], v[208:211], v[246:249], v[48:63]
	v_exp_f32_e32 v211, v90
	v_exp_f32_e32 v208, v92
	v_exp_f32_e32 v210, v93
	v_exp_f32_e32 v209, v95
	v_add_f32_e32 v64, v203, v204
	v_fmac_f32_e32 v64, v197, v140
	v_add_f32_e32 v140, v215, v216
	s_addk_i32 s10, 0x80
	s_add_i32 s64, s64, 2
	s_addk_i32 s11, 0x80
	v_fmac_f32_e32 v140, v64, v206
	s_cbranch_vccz .LBB0_765
	s_and_saveexec_b64 s[8:9], s[4:5]
	ds_write_b32 v189, v205 offset:128
	s_or_b64 exec, exec, s[8:9]
	s_waitcnt lgkmcnt(0)
	v_add_u32_e32 v164, s62, v169
	ds_read_b128 v[238:241], v164 offset:224
	ds_read_b128 v[242:245], v164 offset:192
	ds_read_b128 v[246:249], v164 offset:160
	ds_read_b128 v[250:253], v164 offset:128
	s_waitcnt lgkmcnt(3)
	v_pk_mul_f32 v[28:29], v[28:29], v[238:239]
	s_waitcnt lgkmcnt(2)
	v_pk_mul_f32 v[24:25], v[24:25], v[242:243]
	s_waitcnt lgkmcnt(1)
	v_pk_mul_f32 v[20:21], v[20:21], v[246:247]
	v_pk_mul_f32 v[30:31], v[30:31], v[240:241]
	v_pk_mul_f32 v[26:27], v[26:27], v[244:245]
	v_pk_mul_f32 v[22:23], v[22:23], v[248:249]
	s_waitcnt lgkmcnt(0)
	v_pk_mul_f32 v[18:19], v[18:19], v[252:253]
	v_pk_mul_f32 v[16:17], v[16:17], v[250:251]
	v_pk_mul_f32 v[44:45], v[44:45], v[238:239]
	v_pk_mul_f32 v[40:41], v[40:41], v[242:243]
	v_pk_mul_f32 v[36:37], v[36:37], v[246:247]
	v_pk_mul_f32 v[46:47], v[46:47], v[240:241]
	v_pk_mul_f32 v[42:43], v[42:43], v[244:245]
	v_pk_mul_f32 v[38:39], v[38:39], v[248:249]
	v_pk_mul_f32 v[34:35], v[34:35], v[252:253]
	v_pk_mul_f32 v[32:33], v[32:33], v[250:251]
	v_pk_mul_f32 v[12:13], v[12:13], v[238:239]
	v_pk_mul_f32 v[8:9], v[8:9], v[242:243]
	v_pk_mul_f32 v[4:5], v[4:5], v[246:247]
	v_pk_mul_f32 v[14:15], v[14:15], v[240:241]
	v_pk_mul_f32 v[10:11], v[10:11], v[244:245]
	v_pk_mul_f32 v[6:7], v[6:7], v[248:249]
	v_pk_mul_f32 v[2:3], v[2:3], v[252:253]
	v_pk_mul_f32 v[0:1], v[0:1], v[250:251]
	v_pk_mul_f32 v[60:61], v[60:61], v[238:239]
	v_pk_mul_f32 v[56:57], v[56:57], v[242:243]
	v_pk_mul_f32 v[52:53], v[52:53], v[246:247]
	v_pk_mul_f32 v[62:63], v[62:63], v[240:241]
	v_pk_mul_f32 v[58:59], v[58:59], v[244:245]
	v_pk_mul_f32 v[54:55], v[54:55], v[248:249]
	v_pk_mul_f32 v[50:51], v[50:51], v[252:253]
	v_pk_mul_f32 v[48:49], v[48:49], v[250:251]

.LBB0_2012:
	s_add_i32 s6, 0, 0x12000
	v_add_u32_e32 v199, s6, v170
	v_add_u32_e32 v204, s6, v171
	v_add_u32_e32 v205, s6, v172
	ds_read_b128 v[64:67], v180 offset:49152
	ds_read_b128 v[68:71], v180 offset:57344
	ds_read_b128 v[200:203], v181 offset:49152
	ds_read_b128 v[226:229], v181 offset:57344
	ds_read_b128 v[230:233], v182 offset:49152
	ds_read_b128 v[234:237], v182 offset:57344
	ds_read_b128 v[238:241], v183 offset:49152
	ds_read_b128 v[242:245], v183 offset:57344
	s_waitcnt lgkmcnt(7)
	v_mfma_f32_32x32x16_bf16 v[80:95], v[64:67], v[124:127], 0
	s_add_i32 s8, s8, 2
	s_sub_i32 s80, s14, 64
	s_cmp_lt_u32 s8, 3
	s_cselect_b32 s80, s13, s80
	s_mul_i32 s81, s80, 0xc00
	s_add_i32 s85, s82, 0x8000
	s_mov_b32 m0, s85
	s_add_i32 s85, s82, 0x10000
	buffer_load_dwordx4 v154, s[72:75], s81 offen lds
	v_exp_f32_e32 v216, v128
	v_add_f32_e32 v128, 0, v222
	v_add_f32_e32 v128, v224, v128
	v_add_f32_e32 v128, v220, v128
	v_add_f32_e32 v128, v223, v128
	v_add_f32_e32 v128, v219, v128
	v_add_f32_e32 v128, v221, v128
	s_waitcnt lgkmcnt(6)
	v_mfma_f32_32x32x16_bf16 v[64:79], v[68:71], v[124:127], 0
	s_mov_b32 m0, s85
	s_add_i32 s85, s82, 0xa000
	buffer_load_dwordx4 v155, s[72:75], s81 offen lds
	v_add_f32_e32 v128, v217, v128
	v_add_f32_e32 v128, v218, v128
	v_add_f32_e32 v128, v212, v128
	v_add_f32_e32 v128, v214, v128
	v_add_f32_e32 v128, v211, v128
	v_add_f32_e32 v128, v213, v128
	v_exp_f32_e32 v138, v138
	s_waitcnt lgkmcnt(5)
	v_mfma_f32_32x32x16_bf16 v[80:95], v[200:203], v[120:123], v[80:95]
	s_mov_b32 m0, s85
	s_add_i32 s81, s81, 0x18000
	buffer_load_dwordx4 v154, s[72:75], s81 offen lds
	v_add_f32_e32 v128, v208, v128
	v_exp_f32_e32 v139, v139
	v_add_f32_e32 v128, v210, v128
	v_exp_f32_e32 v164, v136
	v_add_f32_e32 v128, v207, v128
	v_exp_f32_e32 v137, v137
	v_add_f32_e32 v128, v209, v128
	s_waitcnt lgkmcnt(4)
	v_mfma_f32_32x32x16_bf16 v[64:79], v[226:229], v[120:123], v[64:79]
	s_lshl_b32 s81, s83, 11
	s_add_i32 s85, s82, 0x4000
	s_mov_b32 m0, s85
	s_add_i32 s85, s82, 0x6000
	buffer_load_dwordx4 v158, s[76:79], s81 offen lds
	ds_read_b128 v[200:203], v184 offset:49152
	ds_read_b128 v[226:229], v184 offset:57344
	v_exp_f32_e32 v165, v132
	v_add_f32_e32 v128, v138, v128
	v_add_f32_e32 v128, v139, v128
	v_exp_f32_e32 v206, v130
	v_add_f32_e32 v128, v164, v128
	v_exp_f32_e32 v215, v131
	s_waitcnt lgkmcnt(5)
	v_mfma_f32_32x32x16_bf16 v[80:95], v[230:233], v[116:119], v[80:95]
	s_mov_b32 m0, s85
	s_add_i32 s81, s81, 0x10000
	buffer_load_dwordx4 v158, s[76:79], s81 offen lds
	s_mov_b32 s84, s80
	v_add_f32_e32 v128, v137, v128
	v_add_f32_e32 v128, v165, v128
	v_exp_f32_e32 v225, v129
	v_exp_f32_e32 v162, v162
	v_exp_f32_e32 v163, v163
	v_exp_f32_e32 v160, v160
	v_exp_f32_e32 v161, v161
	s_waitcnt lgkmcnt(4)
	v_mfma_f32_32x32x16_bf16 v[64:79], v[234:237], v[116:119], v[64:79]
	ds_read_b128 v[230:233], v185 offset:49152
	ds_read_b128 v[234:237], v185 offset:57344
	v_cvt_pk_bf16_f32 v129, v220, v223
	v_cvt_pk_bf16_f32 v130, v219, v221
	v_cvt_pk_bf16_f32 v131, v217, v218
	v_cvt_pk_bf16_f32 v132, v212, v214
	v_cvt_pk_bf16_f32 v136, v138, v139
	v_cvt_pk_bf16_f32 v137, v164, v137
	s_waitcnt lgkmcnt(5)
	v_mfma_f32_32x32x16_bf16 v[80:95], v[238:241], v[112:115], v[80:95]
	v_cvt_pk_bf16_f32 v139, v206, v215
	v_permlane32_swap_b32_e32 v129, v131
	s_nop 0
	v_permlane32_swap_b32_e32 v137, v139
	s_waitcnt lgkmcnt(4)
	v_mfma_f32_32x32x16_bf16 v[64:79], v[242:245], v[112:115], v[64:79]
	ds_read_b128 v[238:241], v186 offset:49152
	ds_read_b128 v[242:245], v186 offset:57344
	s_waitcnt lgkmcnt(5)
	v_mfma_f32_32x32x16_bf16 v[80:95], v[200:203], v[108:111], v[80:95]
	s_waitcnt lgkmcnt(4)
	v_mfma_f32_32x32x16_bf16 v[64:79], v[226:229], v[108:111], v[64:79]
	ds_read_b128 v[200:203], v187 offset:49152
	ds_read_b128 v[226:229], v187 offset:57344
	s_waitcnt lgkmcnt(5)
	v_mfma_f32_32x32x16_bf16 v[80:95], v[230:233], v[104:107], v[80:95]
	s_waitcnt lgkmcnt(4)
	v_mfma_f32_32x32x16_bf16 v[64:79], v[234:237], v[104:107], v[64:79]
	ds_read_b128 v[230:233], v199
	ds_read_b128 v[234:237], v199 offset:4096
	ds_read_b128 v[246:249], v190
	s_waitcnt lgkmcnt(6)
	v_mfma_f32_32x32x16_bf16 v[80:95], v[238:241], v[100:103], v[80:95]
	s_waitcnt lgkmcnt(5)
	v_mfma_f32_32x32x16_bf16 v[64:79], v[242:245], v[100:103], v[64:79]
	ds_read_b128 v[238:241], v204
	ds_read_b128 v[242:245], v204 offset:4096
	ds_read_b128 v[250:253], v190 offset:1024
	v_add_u32_e32 v204, s6, v173
	s_waitcnt lgkmcnt(7)
	v_mfma_f32_32x32x16_bf16 v[80:95], v[200:203], v[96:99], v[80:95]
	s_waitcnt lgkmcnt(6)
	v_mfma_f32_32x32x16_bf16 v[64:79], v[226:229], v[96:99], v[64:79]
	ds_read_b128 v[200:203], v205
	ds_read_b128 v[226:229], v205 offset:4096
	s_waitcnt lgkmcnt(5)
	v_mfma_f32_32x32x16_bf16 v[80:95], v[230:233], v[246:249], v[80:95]
	s_waitcnt lgkmcnt(5)
	v_mfma_f32_32x32x16_bf16 v[64:79], v[234:237], v[246:249], v[64:79]
	ds_read_b128 v[230:233], v204
	ds_read_b128 v[234:237], v204 offset:4096
	ds_read_b128 v[246:249], v190 offset:2048
	s_waitcnt lgkmcnt(5)
	v_mfma_f32_32x32x16_bf16 v[80:95], v[238:241], v[250:253], v[80:95]
	s_waitcnt lgkmcnt(5)
	v_mfma_f32_32x32x16_bf16 v[64:79], v[242:245], v[250:253], v[64:79]
	ds_read_b128 v[250:253], v190 offset:3072
	s_waitcnt lgkmcnt(1)
	v_mfma_f32_32x32x16_bf16 v[80:95], v[200:203], v[246:249], v[80:95]
	v_exp_f32_e32 v205, v133
	v_cvt_pk_bf16_f32 v133, v211, v213
	v_cvt_pk_bf16_f32 v138, v165, v205
	v_add_f32_e32 v128, v205, v128
	v_add_f32_e32 v128, v206, v128
	v_add_f32_e32 v128, v215, v128
	s_waitcnt lgkmcnt(1)
	v_mfma_f32_32x32x16_bf16 v[64:79], v[226:229], v[246:249], v[64:79]
	v_add_f32_e32 v128, v216, v128
	v_add_f32_e32 v128, v225, v128
	v_add_f32_e32 v128, v162, v128
	v_add_f32_e32 v128, v163, v128
	v_add_f32_e32 v128, v160, v128
	v_add_f32_e32 v128, v161, v128
	s_waitcnt lgkmcnt(0)
	v_mfma_f32_32x32x16_bf16 v[80:95], v[230:233], v[250:253], v[80:95]
	v_exp_f32_e32 v226, v134
	v_exp_f32_e32 v227, v135
	v_cvt_pk_bf16_f32 v134, v208, v210
	v_cvt_pk_bf16_f32 v135, v207, v209
	v_add_f32_e32 v128, v226, v128
	v_add_f32_e32 v203, v227, v128
	v_mov_b32_e32 v204, v203
	s_waitcnt lgkmcnt(0)
	v_mfma_f32_32x32x16_bf16 v[64:79], v[234:237], v[250:253], v[64:79]
	s_nop 0
	v_permlane32_swap_b32_e32 v203, v204
	v_cvt_pk_bf16_f32 v128, v222, v224
	v_cvt_pk_bf16_f32 v208, v216, v225
	v_cvt_pk_bf16_f32 v209, v162, v163
	v_cvt_pk_bf16_f32 v210, v160, v161
	v_cvt_pk_bf16_f32 v211, v226, v227
	v_permlane32_swap_b32_e32 v132, v134
	v_permlane32_swap_b32_e32 v128, v130
	v_permlane32_swap_b32_e32 v133, v135
	v_permlane32_swap_b32_e32 v136, v138
	v_permlane32_swap_b32_e32 v208, v210
	v_permlane32_swap_b32_e32 v209, v211
	ds_read_b64_tr_b16 v[160:161], v167 offset:0
	ds_read_b64_tr_b16 v[162:163], v167 offset:0x800
	ds_read_b64_tr_b16 v[232:233], v167 offset:0x1000
	ds_read_b64_tr_b16 v[234:235], v167 offset:0x1800
	ds_read_b64_tr_b16 v[236:237], v167 offset:0x2000
	ds_read_b64_tr_b16 v[238:239], v167 offset:0x2800
	ds_read_b64_tr_b16 v[240:241], v167 offset:0x3000
	ds_read_b64_tr_b16 v[242:243], v167 offset:0x3800
	v_max_f32_e32 v164, v81, v81
	v_max_f32_e32 v165, v80, v80
	v_max_f32_e32 v164, v165, v164
	v_max3_f32 v164, v164, v82, v83
	v_max3_f32 v164, v164, v84, v85
	v_max3_f32 v164, v164, v86, v87
	v_max3_f32 v164, v164, v88, v89
	v_max3_f32 v164, v164, v90, v91
	v_max3_f32 v164, v164, v92, v93
	v_max3_f32 v164, v164, v94, v95
	s_waitcnt lgkmcnt(6)
	v_mfma_f32_32x32x16_bf16 v[0:15], v[128:131], v[160:163], v[0:15]
	v_max3_f32 v160, v164, v64, v65
	v_max3_f32 v160, v160, v66, v67
	v_max3_f32 v160, v160, v68, v69
	s_waitcnt lgkmcnt(4)
	v_mfma_f32_32x32x16_bf16 v[0:15], v[132:135], v[232:235], v[0:15]
	ds_read_b64_tr_b16 v[232:233], v167 offset:0x200
	ds_read_b64_tr_b16 v[234:235], v167 offset:0xa00
	v_max3_f32 v160, v160, v70, v71
	v_max3_f32 v160, v160, v72, v73
	v_max3_f32 v160, v160, v74, v75
	s_waitcnt lgkmcnt(4)
	v_mfma_f32_32x32x16_bf16 v[0:15], v[136:139], v[236:239], v[0:15]
	ds_read_b64_tr_b16 v[236:237], v167 offset:0x1200
	ds_read_b64_tr_b16 v[238:239], v167 offset:0x1a00
	ds_read_b64_tr_b16 v[244:245], v167 offset:0x2200
	ds_read_b64_tr_b16 v[246:247], v167 offset:0x2a00
	ds_read_b64_tr_b16 v[248:249], v167 offset:0x3200
	ds_read_b64_tr_b16 v[250:251], v167 offset:0x3a00
	v_max3_f32 v160, v160, v76, v77
	v_max3_f32 v160, v160, v78, v79
	v_mov_b32_e32 v161, v160
	s_waitcnt lgkmcnt(8)
	v_mfma_f32_32x32x16_bf16 v[0:15], v[208:211], v[240:243], v[0:15]
	v_max_f32_e32 v162, v198, v198
	v_permlane32_swap_b32_e32 v160, v161
	v_max_f32_e32 v161, v161, v161
	v_max_f32_e32 v160, v160, v160
	v_max_f32_e32 v160, v160, v161
	s_waitcnt lgkmcnt(6)
	v_mfma_f32_32x32x16_bf16 v[32:47], v[128:131], v[232:235], v[32:47]
	ds_read_b64_tr_b16 v[232:233], v167 offset:0x400
	ds_read_b64_tr_b16 v[234:235], v167 offset:0xc00
	v_sub_f32_e32 v161, v160, v198
	v_max_f32_e32 v160, v162, v160
	v_sub_f32_e32 v162, v198, v160
	v_mul_f32_e32 v162, 0x3dd53b94, v162
	v_exp_f32_e32 v162, v162
	s_waitcnt lgkmcnt(6)
	v_mfma_f32_32x32x16_bf16 v[32:47], v[132:135], v[236:239], v[32:47]
	ds_read_b64_tr_b16 v[236:237], v167 offset:0x1400
	ds_read_b64_tr_b16 v[238:239], v167 offset:0x1c00
	ds_read_b64_tr_b16 v[240:241], v167 offset:0x2400
	ds_read_b64_tr_b16 v[242:243], v167 offset:0x2c00
	v_cmp_ge_f32_e32 vcc, s46, v161
	s_cmp_eq_u64 vcc, exec
	s_cselect_b64 s[6:7], -1, 0
	v_cndmask_b32_e64 v206, v162, 1.0, s[6:7]
	v_cndmask_b32_e64 v160, v160, v198, s[6:7]
	v_mul_f32_e32 v205, 0xbdd53b94, v160
	v_cmp_gt_f32_e32 vcc, 1.0, v206
	s_waitcnt lgkmcnt(8)
	v_mfma_f32_32x32x16_bf16 v[32:47], v[136:139], v[244:247], v[32:47]
	ds_read_b64_tr_b16 v[244:245], v167 offset:0x3400
	ds_read_b64_tr_b16 v[246:247], v167 offset:0x3c00
	v_fmamk_f32 v87, v87, 0x3dd53b94, v205
	v_fmamk_f32 v80, v80, 0x3dd53b94, v205
	v_fmamk_f32 v81, v81, 0x3dd53b94, v205
	v_fmamk_f32 v82, v82, 0x3dd53b94, v205
	v_fmamk_f32 v83, v83, 0x3dd53b94, v205
	s_waitcnt lgkmcnt(8)
	v_mfma_f32_32x32x16_bf16 v[32:47], v[208:211], v[248:251], v[32:47]
	v_fmamk_f32 v84, v84, 0x3dd53b94, v205
	v_fmamk_f32 v85, v85, 0x3dd53b94, v205
	v_fmamk_f32 v86, v86, 0x3dd53b94, v205
	v_fmamk_f32 v88, v88, 0x3dd53b94, v205
	v_fmamk_f32 v89, v89, 0x3dd53b94, v205
	s_waitcnt lgkmcnt(6)
	v_mfma_f32_32x32x16_bf16 v[16:31], v[128:131], v[232:235], v[16:31]
	ds_read_b64_tr_b16 v[232:233], v167 offset:0x600
	ds_read_b64_tr_b16 v[234:235], v167 offset:0xe00
	v_fmamk_f32 v90, v90, 0x3dd53b94, v205
	v_fmamk_f32 v91, v91, 0x3dd53b94, v205
	v_fmamk_f32 v92, v92, 0x3dd53b94, v205
	v_fmamk_f32 v93, v93, 0x3dd53b94, v205
	v_fmamk_f32 v94, v94, 0x3dd53b94, v205
	s_waitcnt lgkmcnt(6)
	v_mfma_f32_32x32x16_bf16 v[16:31], v[132:135], v[236:239], v[16:31]
	ds_read_b64_tr_b16 v[236:237], v167 offset:0x1600
	ds_read_b64_tr_b16 v[238:239], v167 offset:0x1e00
	v_fmamk_f32 v95, v95, 0x3dd53b94, v205
	v_fmamk_f32 v215, v64, 0x3dd53b94, v205
	v_fmamk_f32 v216, v65, 0x3dd53b94, v205
	v_fmamk_f32 v217, v66, 0x3dd53b94, v205
	v_fmamk_f32 v218, v67, 0x3dd53b94, v205
	s_waitcnt lgkmcnt(6)
	v_mfma_f32_32x32x16_bf16 v[16:31], v[136:139], v[240:243], v[16:31]
	ds_read_b64_tr_b16 v[240:241], v167 offset:0x2600
	ds_read_b64_tr_b16 v[242:243], v167 offset:0x2e00
	ds_read_b64_tr_b16 v[248:249], v167 offset:0x3600
	ds_read_b64_tr_b16 v[250:251], v167 offset:0x3e00
	v_fmamk_f32 v219, v68, 0x3dd53b94, v205
	v_fmamk_f32 v212, v73, 0x3dd53b94, v205
	v_fmamk_f32 v213, v74, 0x3dd53b94, v205
	v_fmamk_f32 v214, v75, 0x3dd53b94, v205
	s_waitcnt lgkmcnt(8)
	v_mfma_f32_32x32x16_bf16 v[16:31], v[208:211], v[244:247], v[16:31]
	v_fmamk_f32 v207, v76, 0x3dd53b94, v205
	v_fmamk_f32 v220, v77, 0x3dd53b94, v205
	v_fmamk_f32 v221, v78, 0x3dd53b94, v205
	s_waitcnt lgkmcnt(6)
	v_mfma_f32_32x32x16_bf16 v[48:63], v[128:131], v[232:235], v[48:63]
	v_exp_f32_e32 v128, v80
	v_exp_f32_e32 v129, v82
	v_exp_f32_e32 v130, v84
	v_exp_f32_e32 v131, v86
	s_waitcnt lgkmcnt(4)
	v_mfma_f32_32x32x16_bf16 v[48:63], v[132:135], v[236:239], v[48:63]
	v_exp_f32_e32 v132, v88
	v_exp_f32_e32 v133, v90
	v_exp_f32_e32 v134, v92
	v_exp_f32_e32 v135, v94
	s_waitcnt lgkmcnt(2)
	v_mfma_f32_32x32x16_bf16 v[48:63], v[136:139], v[240:243], v[48:63]
	v_exp_f32_e32 v139, v89
	v_exp_f32_e32 v138, v91
	v_exp_f32_e32 v137, v93
	v_exp_f32_e32 v136, v95
	s_waitcnt lgkmcnt(0)
	v_mfma_f32_32x32x16_bf16 v[48:63], v[208:211], v[248:251], v[48:63]
	v_exp_f32_e32 v161, v87
	v_exp_f32_e32 v198, v81
	v_exp_f32_e32 v163, v83
	v_exp_f32_e32 v162, v85
	v_fmamk_f32 v208, v69, 0x3dd53b94, v205
	v_fmamk_f32 v209, v70, 0x3dd53b94, v205
	v_fmamk_f32 v210, v71, 0x3dd53b94, v205
	v_fmamk_f32 v211, v72, 0x3dd53b94, v205
	v_fmac_f32_e32 v205, 0x3dd53b94, v79
	s_cbranch_vccz .LBB0_2016
	s_and_saveexec_b64 s[10:11], s[4:5]
	ds_write_b32 v189, v206 offset:128
	s_or_b64 exec, exec, s[10:11]
	s_waitcnt lgkmcnt(0)
	v_add_u32_e32 v248, s12, v169
	ds_read_b128 v[232:235], v248 offset:224
	ds_read_b128 v[236:239], v248 offset:192
	ds_read_b128 v[240:243], v248 offset:160
	ds_read_b128 v[244:247], v248 offset:128
	s_waitcnt lgkmcnt(3)
	v_pk_mul_f32 v[12:13], v[12:13], v[232:233]
	s_waitcnt lgkmcnt(2)
	v_pk_mul_f32 v[8:9], v[8:9], v[236:237]
	s_waitcnt lgkmcnt(1)
	v_pk_mul_f32 v[4:5], v[4:5], v[240:241]
	v_pk_mul_f32 v[14:15], v[14:15], v[234:235]
	v_pk_mul_f32 v[10:11], v[10:11], v[238:239]
	v_pk_mul_f32 v[6:7], v[6:7], v[242:243]
	s_waitcnt lgkmcnt(0)
	v_pk_mul_f32 v[2:3], v[2:3], v[246:247]
	v_pk_mul_f32 v[0:1], v[0:1], v[244:245]
	v_pk_mul_f32 v[44:45], v[44:45], v[232:233]
	v_pk_mul_f32 v[40:41], v[40:41], v[236:237]
	v_pk_mul_f32 v[36:37], v[36:37], v[240:241]
	v_pk_mul_f32 v[46:47], v[46:47], v[234:235]
	v_pk_mul_f32 v[42:43], v[42:43], v[238:239]
	v_pk_mul_f32 v[38:39], v[38:39], v[242:243]
	v_pk_mul_f32 v[34:35], v[34:35], v[246:247]
	v_pk_mul_f32 v[32:33], v[32:33], v[244:245]
	v_pk_mul_f32 v[28:29], v[28:29], v[232:233]
	v_pk_mul_f32 v[24:25], v[24:25], v[236:237]
	v_pk_mul_f32 v[20:21], v[20:21], v[240:241]
	v_pk_mul_f32 v[30:31], v[30:31], v[234:235]
	v_pk_mul_f32 v[26:27], v[26:27], v[238:239]
	v_pk_mul_f32 v[22:23], v[22:23], v[242:243]
	v_pk_mul_f32 v[18:19], v[18:19], v[246:247]
	v_pk_mul_f32 v[16:17], v[16:17], v[244:245]
	v_pk_mul_f32 v[60:61], v[60:61], v[232:233]
	v_pk_mul_f32 v[56:57], v[56:57], v[236:237]
	v_pk_mul_f32 v[52:53], v[52:53], v[240:241]
	v_pk_mul_f32 v[62:63], v[62:63], v[234:235]
	v_pk_mul_f32 v[58:59], v[58:59], v[238:239]
	v_pk_mul_f32 v[54:55], v[54:55], v[242:243]
	v_pk_mul_f32 v[50:51], v[50:51], v[246:247]
	v_pk_mul_f32 v[48:49], v[48:49], v[244:245]
.LBB0_2016:
	s_waitcnt vmcnt(0) lgkmcnt(0)
	s_barrier
	ds_read_b128 v[64:67], v180 offset:32768
	ds_read_b128 v[68:71], v180 offset:40960
	ds_read_b128 v[222:225], v181 offset:32768
	ds_read_b128 v[226:229], v181 offset:40960
	ds_read_b128 v[230:233], v182 offset:32768
	ds_read_b128 v[234:237], v182 offset:40960
	ds_read_b128 v[238:241], v183 offset:32768
	ds_read_b128 v[242:245], v183 offset:40960
	v_exp_f32_e32 v164, v215
	v_add_f32_e32 v215, 0, v128
	s_waitcnt lgkmcnt(7)
	v_mfma_f32_32x32x16_bf16 v[80:95], v[64:67], v[124:127], 0
	s_add_i32 s80, s13, 64
	s_cmp_lt_u32 s8, 2
	s_cselect_b32 s80, s80, s14
	s_mul_i32 s81, s80, 0xc00
	s_add_i32 s85, s82, 0xc000
	s_mov_b32 m0, s85
	s_add_i32 s85, s82, 0x12000
	buffer_load_dwordx4 v154, s[72:75], s81 offen lds
	v_add_f32_e32 v215, v198, v215
	v_add_f32_e32 v215, v129, v215
	v_add_f32_e32 v215, v163, v215
	v_add_f32_e32 v215, v130, v215
	v_add_f32_e32 v215, v162, v215
	v_add_f32_e32 v215, v131, v215
	v_add_f32_e32 v215, v161, v215
	s_waitcnt lgkmcnt(6)
	v_mfma_f32_32x32x16_bf16 v[64:79], v[68:71], v[124:127], 0
	s_mov_b32 m0, s85
	s_add_i32 s85, s82, 0xe000
	buffer_load_dwordx4 v155, s[72:75], s81 offen lds
	v_add_f32_e32 v215, v132, v215
	v_add_f32_e32 v215, v139, v215
	v_add_f32_e32 v215, v133, v215
	v_add_f32_e32 v215, v138, v215
	v_add_f32_e32 v215, v134, v215
	v_exp_f32_e32 v165, v216
	v_add_f32_e32 v215, v137, v215
	s_waitcnt lgkmcnt(5)
	v_mfma_f32_32x32x16_bf16 v[80:95], v[222:225], v[120:123], v[80:95]
	s_mov_b32 m0, s85
	s_add_i32 s81, s81, 0x18000
	buffer_load_dwordx4 v154, s[72:75], s81 offen lds
	v_exp_f32_e32 v217, v217
	v_add_f32_e32 v215, v135, v215
	v_exp_f32_e32 v218, v218
	v_add_f32_e32 v215, v136, v215
	v_exp_f32_e32 v219, v219
	v_add_f32_e32 v215, v164, v215
	v_exp_f32_e32 v208, v208
	s_waitcnt lgkmcnt(4)
	v_mfma_f32_32x32x16_bf16 v[64:79], v[226:229], v[120:123], v[64:79]
	s_lshl_b32 s81, s84, 11
	s_add_i32 s85, s82, 0x0
	s_mov_b32 m0, s85
	s_add_i32 s85, s82, 0x2000
	buffer_load_dwordx4 v158, s[76:79], s81 offen lds
	ds_read_b128 v[222:225], v184 offset:32768
	ds_read_b128 v[226:229], v184 offset:40960
	v_add_f32_e32 v215, v165, v215
	v_exp_f32_e32 v209, v209
	v_add_f32_e32 v215, v217, v215
	v_exp_f32_e32 v210, v210
	v_add_f32_e32 v215, v218, v215
	v_exp_f32_e32 v211, v211
	s_waitcnt lgkmcnt(5)
	v_mfma_f32_32x32x16_bf16 v[80:95], v[230:233], v[116:119], v[80:95]
	s_mov_b32 m0, s85
	s_add_i32 s81, s81, 0x10000
	buffer_load_dwordx4 v158, s[76:79], s81 offen lds
	s_mov_b32 s83, s80
	v_add_f32_e32 v215, v219, v215
	v_exp_f32_e32 v212, v212
	v_add_f32_e32 v215, v208, v215
	v_exp_f32_e32 v213, v213
	v_add_f32_e32 v215, v209, v215
	v_exp_f32_e32 v214, v214
	v_add_f32_e32 v215, v210, v215
	s_waitcnt lgkmcnt(4)
	v_mfma_f32_32x32x16_bf16 v[64:79], v[234:237], v[116:119], v[64:79]
	ds_read_b128 v[230:233], v185 offset:32768
	ds_read_b128 v[234:237], v185 offset:40960
	v_exp_f32_e32 v207, v207
	v_add_f32_e32 v215, v211, v215
	v_exp_f32_e32 v220, v220
	v_add_f32_e32 v215, v212, v215
	v_exp_f32_e32 v221, v221
	v_add_f32_e32 v215, v213, v215
	s_waitcnt lgkmcnt(5)
	v_mfma_f32_32x32x16_bf16 v[80:95], v[238:241], v[112:115], v[80:95]
	v_exp_f32_e32 v205, v205
	v_add_f32_e32 v215, v214, v215
	v_add_f32_e32 v215, v207, v215
	v_add_f32_e32 v215, v220, v215
	v_add_f32_e32 v215, v221, v215
	v_add_f32_e32 v215, v205, v215
	v_mov_b32_e32 v216, v215
	s_waitcnt lgkmcnt(4)
	v_mfma_f32_32x32x16_bf16 v[64:79], v[242:245], v[112:115], v[64:79]
	ds_read_b128 v[238:241], v186 offset:32768
	ds_read_b128 v[242:245], v186 offset:40960
	v_permlane32_swap_b32_e32 v215, v216
	v_cvt_pk_bf16_f32 v128, v128, v198
	v_cvt_pk_bf16_f32 v129, v129, v163
	v_cvt_pk_bf16_f32 v130, v130, v162
	v_cvt_pk_bf16_f32 v131, v131, v161
	s_waitcnt lgkmcnt(5)
	v_mfma_f32_32x32x16_bf16 v[80:95], v[222:225], v[108:111], v[80:95]
	v_cvt_pk_bf16_f32 v132, v132, v139
	v_cvt_pk_bf16_f32 v133, v133, v138
	v_cvt_pk_bf16_f32 v134, v134, v137
	v_cvt_pk_bf16_f32 v135, v135, v136
	v_cvt_pk_bf16_f32 v136, v164, v165
	v_cvt_pk_bf16_f32 v137, v217, v218
	v_cvt_pk_bf16_f32 v138, v219, v208
	s_waitcnt lgkmcnt(4)
	v_mfma_f32_32x32x16_bf16 v[64:79], v[226:229], v[108:111], v[64:79]
	ds_read_b128 v[222:225], v187 offset:32768
	ds_read_b128 v[226:229], v187 offset:40960
	v_cvt_pk_bf16_f32 v139, v209, v210
	v_cvt_pk_bf16_f32 v208, v211, v212
	v_cvt_pk_bf16_f32 v209, v213, v214
	v_cvt_pk_bf16_f32 v210, v207, v220
	v_cvt_pk_bf16_f32 v211, v221, v205
	v_permlane32_swap_b32_e32 v128, v130
	s_waitcnt lgkmcnt(5)
	v_mfma_f32_32x32x16_bf16 v[80:95], v[230:233], v[104:107], v[80:95]
	v_permlane32_swap_b32_e32 v129, v131
	v_permlane32_swap_b32_e32 v132, v134
	v_permlane32_swap_b32_e32 v133, v135
	v_permlane32_swap_b32_e32 v136, v138
	s_waitcnt lgkmcnt(4)
	v_mfma_f32_32x32x16_bf16 v[64:79], v[234:237], v[104:107], v[64:79]
	ds_read_b128 v[230:233], v191
	ds_read_b128 v[234:237], v191 offset:4096
	ds_read_b128 v[246:249], v190
	v_permlane32_swap_b32_e32 v137, v139
	v_permlane32_swap_b32_e32 v208, v210
	v_permlane32_swap_b32_e32 v209, v211
	s_waitcnt lgkmcnt(6)
	v_mfma_f32_32x32x16_bf16 v[80:95], v[238:241], v[100:103], v[80:95]
	s_waitcnt lgkmcnt(5)
	v_mfma_f32_32x32x16_bf16 v[64:79], v[242:245], v[100:103], v[64:79]
	ds_read_b128 v[238:241], v192
	ds_read_b128 v[242:245], v192 offset:4096
	ds_read_b128 v[250:253], v190 offset:1024
	s_waitcnt lgkmcnt(7)
	v_mfma_f32_32x32x16_bf16 v[80:95], v[222:225], v[96:99], v[80:95]
	s_waitcnt lgkmcnt(6)
	v_mfma_f32_32x32x16_bf16 v[64:79], v[226:229], v[96:99], v[64:79]
	ds_read_b128 v[222:225], v193
	ds_read_b128 v[226:229], v193 offset:4096
	s_waitcnt lgkmcnt(5)
	v_mfma_f32_32x32x16_bf16 v[80:95], v[230:233], v[246:249], v[80:95]
	s_waitcnt lgkmcnt(5)
	v_mfma_f32_32x32x16_bf16 v[64:79], v[234:237], v[246:249], v[64:79]
	ds_read_b128 v[230:233], v194
	ds_read_b128 v[234:237], v194 offset:4096
	ds_read_b128 v[246:249], v190 offset:2048
	s_waitcnt lgkmcnt(5)
	v_mfma_f32_32x32x16_bf16 v[80:95], v[238:241], v[250:253], v[80:95]
	s_waitcnt lgkmcnt(5)
	v_mfma_f32_32x32x16_bf16 v[64:79], v[242:245], v[250:253], v[64:79]
	ds_read_b128 v[250:253], v190 offset:3072
	s_waitcnt lgkmcnt(1)
	v_mfma_f32_32x32x16_bf16 v[80:95], v[222:225], v[246:249], v[80:95]
	s_waitcnt lgkmcnt(1)
	v_mfma_f32_32x32x16_bf16 v[64:79], v[226:229], v[246:249], v[64:79]
	s_waitcnt lgkmcnt(0)
	v_mfma_f32_32x32x16_bf16 v[80:95], v[230:233], v[250:253], v[80:95]
	s_waitcnt lgkmcnt(0)
	v_mfma_f32_32x32x16_bf16 v[64:79], v[234:237], v[250:253], v[64:79]
	ds_read_b64_tr_b16 v[238:239], v174 offset:0
	ds_read_b64_tr_b16 v[240:241], v174 offset:0x800
	ds_read_b64_tr_b16 v[242:243], v174 offset:0x1000
	ds_read_b64_tr_b16 v[244:245], v174 offset:0x1800
	ds_read_b64_tr_b16 v[246:247], v174 offset:0x2000
	ds_read_b64_tr_b16 v[248:249], v174 offset:0x2800
	ds_read_b64_tr_b16 v[250:251], v174 offset:0x3000
	ds_read_b64_tr_b16 v[252:253], v174 offset:0x3800
	s_nop 3
	v_max_f32_e32 v161, v81, v81
	v_max_f32_e32 v162, v80, v80
	v_max_f32_e32 v161, v162, v161
	v_max3_f32 v161, v161, v82, v83
	v_max3_f32 v161, v161, v84, v85
	v_max3_f32 v161, v161, v86, v87
	v_max3_f32 v161, v161, v88, v89
	v_max3_f32 v161, v161, v90, v91
	v_max3_f32 v161, v161, v92, v93
	v_max3_f32 v161, v161, v94, v95
	s_waitcnt lgkmcnt(6)
	v_mfma_f32_32x32x16_bf16 v[0:15], v[128:131], v[238:241], v[0:15]
	ds_read_b64_tr_b16 v[238:239], v174 offset:0x200
	ds_read_b64_tr_b16 v[240:241], v174 offset:0xa00
	v_max3_f32 v161, v161, v64, v65
	v_max3_f32 v161, v161, v66, v67
	v_max3_f32 v161, v161, v68, v69
	s_waitcnt lgkmcnt(6)
	v_mfma_f32_32x32x16_bf16 v[0:15], v[132:135], v[242:245], v[0:15]
	ds_read_b64_tr_b16 v[242:243], v174 offset:0x1200
	ds_read_b64_tr_b16 v[244:245], v174 offset:0x1a00
	v_max3_f32 v161, v161, v70, v71
	v_max3_f32 v161, v161, v72, v73
	v_max3_f32 v161, v161, v74, v75
	s_waitcnt lgkmcnt(6)
	v_mfma_f32_32x32x16_bf16 v[0:15], v[136:139], v[246:249], v[0:15]
	ds_read_b64_tr_b16 v[246:247], v174 offset:0x2200
	ds_read_b64_tr_b16 v[248:249], v174 offset:0x2a00
	ds_read_b64_tr_b16 v[162:163], v174 offset:0x3200
	ds_read_b64_tr_b16 v[164:165], v174 offset:0x3a00
	v_max3_f32 v161, v161, v76, v77
	v_max3_f32 v161, v161, v78, v79
	v_mov_b32_e32 v198, v161
	s_waitcnt lgkmcnt(8)
	v_mfma_f32_32x32x16_bf16 v[0:15], v[208:211], v[250:253], v[0:15]
	v_max_f32_e32 v205, v160, v160
	v_permlane32_swap_b32_e32 v161, v198
	v_max_f32_e32 v198, v198, v198
	v_max_f32_e32 v161, v161, v161
	v_max_f32_e32 v161, v161, v198
	s_waitcnt lgkmcnt(6)
	v_mfma_f32_32x32x16_bf16 v[32:47], v[128:131], v[238:241], v[32:47]
	ds_read_b64_tr_b16 v[238:239], v174 offset:0x400
	ds_read_b64_tr_b16 v[240:241], v174 offset:0xc00
	v_sub_f32_e32 v198, v161, v160
	v_max_f32_e32 v161, v205, v161
	v_sub_f32_e32 v205, v160, v161
	v_mul_f32_e32 v205, 0x3dd53b94, v205
	v_exp_f32_e32 v205, v205
	s_waitcnt lgkmcnt(6)
	v_mfma_f32_32x32x16_bf16 v[32:47], v[132:135], v[242:245], v[32:47]
	ds_read_b64_tr_b16 v[242:243], v174 offset:0x1400
	ds_read_b64_tr_b16 v[244:245], v174 offset:0x1c00
	v_cmp_ge_f32_e32 vcc, s46, v198
	s_cmp_eq_u64 vcc, exec
	s_cselect_b64 s[6:7], -1, 0
	v_cndmask_b32_e64 v205, v205, 1.0, s[6:7]
	v_cndmask_b32_e64 v198, v161, v160, s[6:7]
	v_mul_f32_e32 v236, 0xbdd53b94, v198
	v_mov_b32_e32 v237, v236
	v_cmp_gt_f32_e32 vcc, 1.0, v205
	s_waitcnt lgkmcnt(6)
	v_mfma_f32_32x32x16_bf16 v[32:47], v[136:139], v[246:249], v[32:47]
	ds_read_b64_tr_b16 v[246:247], v174 offset:0x2400
	ds_read_b64_tr_b16 v[248:249], v174 offset:0x2c00
	ds_read_b64_tr_b16 v[250:251], v174 offset:0x3400
	ds_read_b64_tr_b16 v[252:253], v174 offset:0x3c00
	v_fmamk_f32 v80, v80, 0x3dd53b94, v236
	v_fmamk_f32 v81, v81, 0x3dd53b94, v236
	v_fmamk_f32 v82, v82, 0x3dd53b94, v236
	v_fmamk_f32 v83, v83, 0x3dd53b94, v236
	s_waitcnt lgkmcnt(8)
	v_mfma_f32_32x32x16_bf16 v[32:47], v[208:211], v[162:165], v[32:47]
	v_fmamk_f32 v84, v84, 0x3dd53b94, v236
	v_fmamk_f32 v85, v85, 0x3dd53b94, v236
	v_fmamk_f32 v86, v86, 0x3dd53b94, v236
	v_fmamk_f32 v87, v87, 0x3dd53b94, v236
	s_waitcnt lgkmcnt(6)
	v_mfma_f32_32x32x16_bf16 v[16:31], v[128:131], v[238:241], v[16:31]
	ds_read_b64_tr_b16 v[162:163], v174 offset:0x600
	ds_read_b64_tr_b16 v[164:165], v174 offset:0xe00
	ds_read_b64_tr_b16 v[238:239], v174 offset:0x1600
	ds_read_b64_tr_b16 v[240:241], v174 offset:0x1e00
	v_fmamk_f32 v88, v88, 0x3dd53b94, v236
	v_fmamk_f32 v89, v89, 0x3dd53b94, v236
	v_fmamk_f32 v90, v90, 0x3dd53b94, v236
	v_fmamk_f32 v91, v91, 0x3dd53b94, v236
	s_waitcnt lgkmcnt(8)
	v_mfma_f32_32x32x16_bf16 v[16:31], v[132:135], v[242:245], v[16:31]
	ds_read_b64_tr_b16 v[242:243], v174 offset:0x2600
	ds_read_b64_tr_b16 v[244:245], v174 offset:0x2e00
	v_fmamk_f32 v92, v92, 0x3dd53b94, v236
	v_fmamk_f32 v93, v93, 0x3dd53b94, v236
	v_fmamk_f32 v94, v94, 0x3dd53b94, v236
	v_fmamk_f32 v95, v95, 0x3dd53b94, v236
	s_waitcnt lgkmcnt(8)
	v_mfma_f32_32x32x16_bf16 v[16:31], v[136:139], v[246:249], v[16:31]
	ds_read_b64_tr_b16 v[246:247], v174 offset:0x3600
	ds_read_b64_tr_b16 v[248:249], v174 offset:0x3e00
	v_exp_f32_e32 v222, v80
	v_exp_f32_e32 v224, v81
	v_exp_f32_e32 v220, v82
	s_waitcnt lgkmcnt(8)
	v_mfma_f32_32x32x16_bf16 v[16:31], v[208:211], v[250:253], v[16:31]
	v_exp_f32_e32 v223, v83
	v_exp_f32_e32 v219, v84
	v_exp_f32_e32 v221, v85
	s_waitcnt lgkmcnt(6)
	v_mfma_f32_32x32x16_bf16 v[48:63], v[128:131], v[162:165], v[48:63]
	v_exp_f32_e32 v217, v86
	v_exp_f32_e32 v218, v87
	v_exp_f32_e32 v212, v88
	v_pk_fma_f32 v[130:131], v[70:71], s[26:27], v[236:237] op_sel_hi:[1,0,0]
	v_pk_fma_f32 v[128:129], v[72:73], s[26:27], v[236:237] op_sel_hi:[1,0,0]
	s_waitcnt lgkmcnt(4)
	v_mfma_f32_32x32x16_bf16 v[48:63], v[132:135], v[238:241], v[48:63]
	v_exp_f32_e32 v214, v89
	v_exp_f32_e32 v213, v91
	v_exp_f32_e32 v207, v94
	v_pk_fma_f32 v[132:133], v[68:69], s[26:27], v[236:237] op_sel_hi:[1,0,0]
	v_pk_fma_f32 v[134:135], v[78:79], s[26:27], v[236:237] op_sel_hi:[1,0,0]
	s_waitcnt lgkmcnt(2)
	v_mfma_f32_32x32x16_bf16 v[48:63], v[136:139], v[242:245], v[48:63]
	v_pk_fma_f32 v[138:139], v[64:65], s[26:27], v[236:237] op_sel_hi:[1,0,0]
	v_pk_fma_f32 v[136:137], v[66:67], s[26:27], v[236:237] op_sel_hi:[1,0,0]
	v_pk_fma_f32 v[162:163], v[74:75], s[26:27], v[236:237] op_sel_hi:[1,0,0]
	v_pk_fma_f32 v[160:161], v[76:77], s[26:27], v[236:237] op_sel_hi:[1,0,0]
	s_waitcnt lgkmcnt(0)
	v_mfma_f32_32x32x16_bf16 v[48:63], v[208:211], v[246:249], v[48:63]
	v_exp_f32_e32 v211, v90
	v_exp_f32_e32 v208, v92
	v_exp_f32_e32 v210, v93
	v_exp_f32_e32 v209, v95
	v_add_f32_e32 v64, v203, v204
	v_fmac_f32_e32 v64, v197, v140
	v_add_f32_e32 v140, v215, v216
	s_addk_i32 s13, 0x80
	s_addk_i32 s14, 0x80
	v_fmac_f32_e32 v140, v64, v206
	s_cbranch_vccz .LBB0_2020
	s_and_saveexec_b64 s[10:11], s[4:5]
	ds_write_b32 v189, v205 offset:128
	s_or_b64 exec, exec, s[10:11]
	s_waitcnt lgkmcnt(0)
	v_add_u32_e32 v164, s12, v169
	ds_read_b128 v[238:241], v164 offset:224
	ds_read_b128 v[242:245], v164 offset:192
	ds_read_b128 v[246:249], v164 offset:160
	ds_read_b128 v[250:253], v164 offset:128
	s_waitcnt lgkmcnt(3)
	v_pk_mul_f32 v[12:13], v[12:13], v[238:239]
	s_waitcnt lgkmcnt(2)
	v_pk_mul_f32 v[8:9], v[8:9], v[242:243]
	s_waitcnt lgkmcnt(1)
	v_pk_mul_f32 v[4:5], v[4:5], v[246:247]
	v_pk_mul_f32 v[14:15], v[14:15], v[240:241]
	v_pk_mul_f32 v[10:11], v[10:11], v[244:245]
	v_pk_mul_f32 v[6:7], v[6:7], v[248:249]
	s_waitcnt lgkmcnt(0)
	v_pk_mul_f32 v[2:3], v[2:3], v[252:253]
	v_pk_mul_f32 v[0:1], v[0:1], v[250:251]
	v_pk_mul_f32 v[44:45], v[44:45], v[238:239]
	v_pk_mul_f32 v[40:41], v[40:41], v[242:243]
	v_pk_mul_f32 v[36:37], v[36:37], v[246:247]
	v_pk_mul_f32 v[46:47], v[46:47], v[240:241]
	v_pk_mul_f32 v[42:43], v[42:43], v[244:245]
	v_pk_mul_f32 v[38:39], v[38:39], v[248:249]
	v_pk_mul_f32 v[34:35], v[34:35], v[252:253]
	v_pk_mul_f32 v[32:33], v[32:33], v[250:251]
	v_pk_mul_f32 v[28:29], v[28:29], v[238:239]
	v_pk_mul_f32 v[24:25], v[24:25], v[242:243]
	v_pk_mul_f32 v[20:21], v[20:21], v[246:247]
	v_pk_mul_f32 v[30:31], v[30:31], v[240:241]
	v_pk_mul_f32 v[26:27], v[26:27], v[244:245]
	v_pk_mul_f32 v[22:23], v[22:23], v[248:249]
	v_pk_mul_f32 v[18:19], v[18:19], v[252:253]
	v_pk_mul_f32 v[16:17], v[16:17], v[250:251]
	v_pk_mul_f32 v[60:61], v[60:61], v[238:239]
	v_pk_mul_f32 v[56:57], v[56:57], v[242:243]
	v_pk_mul_f32 v[52:53], v[52:53], v[246:247]
	v_pk_mul_f32 v[62:63], v[62:63], v[240:241]
	v_pk_mul_f32 v[58:59], v[58:59], v[244:245]
	v_pk_mul_f32 v[54:55], v[54:55], v[248:249]
	v_pk_mul_f32 v[50:51], v[50:51], v[252:253]
	v_pk_mul_f32 v[48:49], v[48:49], v[250:251]
